# accumulator zeroing with 64-bit moves; dropped redundant zero-init before paired fp8 converts in the weight-conversion stash
# speedup vs baseline: 1.0144x; 1.0016x over previous
; #define PG8_BAR __builtin_amdgcn_s_barrier()
; template <bool F8 = false, class Epi, class Sched, class AB>
; __device__ __forceinline__ void gemm_phase(LAS unsigned char* lds, int KB, const Sched& S, const AB& P, const Epi& E, int wave_) {
;     ...
; #pragma unroll
;         for (int a = 0; a < 2; ++a)
; #pragma unroll
;             for (int b = 0; b < 2; ++b)
; #pragma unroll
;                 for (int m = 0; m < 4; ++m)
; #pragma unroll
;                     for (int n = 0; n < 2; ++n) acc[a][b][m][n] = (f32x4){0.f, 0.f, 0.f, 0.f};
;         cur = nxt; cA = nA; cB = nB; ++ui;
; #pragma unroll
;         for (int i = 0; i < 4; ++i) cvo[i] = nvo[i];
;         if (wr == 1) PG8_BAR;
.LBB0_319:
	s_add_u32 s5, s30, 0x100
	v_mov_b32_e32 v0, 0
	s_addc_u32 s6, s31, 0
	s_mov_b32 s21, -2
	v_mov_b64_e32 v[0:1], 0
	v_mov_b64_e32 v[2:3], 0
	v_mov_b64_e32 v[4:5], 0
	v_mov_b64_e32 v[6:7], 0
	v_mov_b64_e32 v[8:9], 0
	v_mov_b64_e32 v[10:11], 0
	v_mov_b64_e32 v[12:13], 0
	v_mov_b64_e32 v[14:15], 0
	v_mov_b64_e32 v[16:17], 0
	v_mov_b64_e32 v[18:19], 0
	v_mov_b64_e32 v[20:21], 0
	v_mov_b64_e32 v[22:23], 0
	v_mov_b64_e32 v[24:25], 0
	v_mov_b64_e32 v[26:27], 0
	v_mov_b64_e32 v[28:29], 0
	v_mov_b64_e32 v[30:31], 0
	v_mov_b64_e32 v[32:33], 0
	v_mov_b64_e32 v[34:35], 0
	v_mov_b64_e32 v[36:37], 0
	v_mov_b64_e32 v[38:39], 0
	v_mov_b64_e32 v[40:41], 0
	v_mov_b64_e32 v[42:43], 0
	v_mov_b64_e32 v[44:45], 0
	v_mov_b64_e32 v[46:47], 0
	v_mov_b64_e32 v[48:49], 0
	v_mov_b64_e32 v[50:51], 0
	v_mov_b64_e32 v[52:53], 0
	v_mov_b64_e32 v[54:55], 0
	v_mov_b64_e32 v[56:57], 0
	v_mov_b64_e32 v[58:59], 0
	v_mov_b64_e32 v[60:61], 0
	v_mov_b64_e32 v[62:63], 0
	v_mov_b64_e32 v[64:65], 0
	v_mov_b64_e32 v[66:67], 0
	v_mov_b64_e32 v[68:69], 0
	v_mov_b64_e32 v[70:71], 0
	v_mov_b64_e32 v[72:73], 0
	v_mov_b64_e32 v[74:75], 0
	v_mov_b64_e32 v[76:77], 0
	v_mov_b64_e32 v[78:79], 0
	v_mov_b64_e32 v[80:81], 0
	v_mov_b64_e32 v[82:83], 0
	v_mov_b64_e32 v[84:85], 0
	v_mov_b64_e32 v[86:87], 0
	v_mov_b64_e32 v[88:89], 0
	v_mov_b64_e32 v[90:91], 0
	v_mov_b64_e32 v[92:93], 0
	v_mov_b64_e32 v[94:95], 0
	v_mov_b64_e32 v[96:97], 0
	v_mov_b64_e32 v[98:99], 0
	v_mov_b64_e32 v[100:101], 0
	v_mov_b64_e32 v[102:103], 0
	v_mov_b64_e32 v[104:105], 0
	v_mov_b64_e32 v[106:107], 0
	v_mov_b64_e32 v[108:109], 0
	v_mov_b64_e32 v[110:111], 0
	v_mov_b64_e32 v[112:113], 0
	v_mov_b64_e32 v[114:115], 0
	v_mov_b64_e32 v[116:117], 0
	v_mov_b64_e32 v[118:119], 0
	v_mov_b64_e32 v[120:121], 0
	v_mov_b64_e32 v[122:123], 0
	v_mov_b64_e32 v[124:125], 0
	v_mov_b64_e32 v[126:127], 0

; #define PG8_BAR __builtin_amdgcn_s_barrier()
; template <bool F8 = false, class Epi, class Sched, class AB>
; __device__ __forceinline__ void gemm_phase(LAS unsigned char* lds, int KB, const Sched& S, const AB& P, const Epi& E, int wave_) {
;     ...
; #pragma unroll
;         for (int a = 0; a < 2; ++a)
; #pragma unroll
;             for (int b = 0; b < 2; ++b)
; #pragma unroll
;                 for (int m = 0; m < 4; ++m)
; #pragma unroll
;                     for (int n = 0; n < 2; ++n) acc[a][b][m][n] = (f32x4){0.f, 0.f, 0.f, 0.f};
;         cur = nxt; cA = nA; cB = nB; ++ui;
; #pragma unroll
;         for (int i = 0; i < 4; ++i) cvo[i] = nvo[i];
;         if (wr == 1) PG8_BAR;
.LBB0_554:
	s_add_u32 s38, s38, 0x80
	s_addc_u32 s39, s39, 0
	s_add_u32 s3, s40, 0x100
	v_mov_b32_e32 v32, 0
	s_addc_u32 s5, s41, 0
	s_mov_b32 s6, -2
	v_mov_b64_e32 v[32:33], 0
	v_mov_b64_e32 v[34:35], 0
	v_mov_b64_e32 v[36:37], 0
	v_mov_b64_e32 v[38:39], 0
	v_mov_b64_e32 v[40:41], 0
	v_mov_b64_e32 v[42:43], 0
	v_mov_b64_e32 v[44:45], 0
	v_mov_b64_e32 v[46:47], 0
	v_mov_b64_e32 v[48:49], 0
	v_mov_b64_e32 v[50:51], 0
	v_mov_b64_e32 v[52:53], 0
	v_mov_b64_e32 v[54:55], 0
	v_mov_b64_e32 v[56:57], 0
	v_mov_b64_e32 v[58:59], 0
	v_mov_b64_e32 v[60:61], 0
	v_mov_b64_e32 v[62:63], 0
	v_mov_b64_e32 v[64:65], 0
	v_mov_b64_e32 v[66:67], 0
	v_mov_b64_e32 v[68:69], 0
	v_mov_b64_e32 v[70:71], 0
	v_mov_b64_e32 v[72:73], 0
	v_mov_b64_e32 v[74:75], 0
	v_mov_b64_e32 v[76:77], 0
	v_mov_b64_e32 v[78:79], 0
	v_mov_b64_e32 v[80:81], 0
	v_mov_b64_e32 v[82:83], 0
	v_mov_b64_e32 v[84:85], 0
	v_mov_b64_e32 v[86:87], 0
	v_mov_b64_e32 v[88:89], 0
	v_mov_b64_e32 v[90:91], 0
	v_mov_b64_e32 v[92:93], 0
	v_mov_b64_e32 v[94:95], 0
	v_mov_b64_e32 v[96:97], 0
	v_mov_b64_e32 v[98:99], 0
	v_mov_b64_e32 v[100:101], 0
	v_mov_b64_e32 v[102:103], 0
	v_mov_b64_e32 v[104:105], 0
	v_mov_b64_e32 v[106:107], 0
	v_mov_b64_e32 v[108:109], 0
	v_mov_b64_e32 v[110:111], 0
	v_mov_b64_e32 v[112:113], 0
	v_mov_b64_e32 v[114:115], 0
	v_mov_b64_e32 v[116:117], 0
	v_mov_b64_e32 v[118:119], 0
	v_mov_b64_e32 v[120:121], 0
	v_mov_b64_e32 v[122:123], 0
	v_mov_b64_e32 v[124:125], 0
	v_mov_b64_e32 v[126:127], 0
	v_mov_b64_e32 v[128:129], 0
	v_mov_b64_e32 v[130:131], 0
	v_mov_b64_e32 v[132:133], 0
	v_mov_b64_e32 v[134:135], 0
	v_mov_b64_e32 v[136:137], 0
	v_mov_b64_e32 v[138:139], 0
	v_mov_b64_e32 v[140:141], 0
	v_mov_b64_e32 v[142:143], 0
	v_mov_b64_e32 v[144:145], 0
	v_mov_b64_e32 v[146:147], 0
	v_mov_b64_e32 v[148:149], 0
	v_mov_b64_e32 v[150:151], 0
	v_mov_b64_e32 v[152:153], 0
	v_mov_b64_e32 v[154:155], 0
	v_mov_b64_e32 v[156:157], 0
	v_mov_b64_e32 v[158:159], 0

; #define LAS __attribute__((address_space(3)))
; __device__ __forceinline__ unsigned cvt4_fp8(float a, float b, float c, float d) { int w = 0; w = __builtin_amdgcn_cvt_pk_fp8_f32(a, b, w, false); w = __builtin_amdgcn_cvt_pk_fp8_f32(c, d, w, true); return (unsigned)w; }
; #define LDS_WAIT() asm volatile("s_waitcnt lgkmcnt(0)" ::: "memory")
; __device__ __forceinline__ void cv_emit(unsigned char* dst, int lane, const f32x4 (&t)[8], LAS unsigned* scr) {
;     { const int lr = lane >> 3, c4 = lane & 7;
; #pragma unroll
;       for (int i = 0; i < 8; ++i) { const f32x4 v = t[i] * F8_WSCALE; scr[(8 * i + lr) * 9 + c4] = cvt4_fp8(v[0], v[1], v[2], v[3]); } }
;     LDS_WAIT(); asm volatile("" ::: "memory");
;     const int cc = lane & 7, nq = lane >> 5, sh = (lane >> 3) & 3;
;     const unsigned selA = (unsigned)sh | ((4u + (unsigned)sh) << 8);
; #pragma unroll
;     for (int j = 0; j < 4; ++j) { const LAS unsigned* p = scr + (8 * cc) * 9 + nq + 2 * j;
;         const unsigned d0 = p[0], d1 = p[9], d2 = p[18], d3 = p[27], d4 = p[36], d5 = p[45], d6 = p[54], d7 = p[63];
;         const unsigned p01 = __builtin_amdgcn_perm(d1, d0, selA), p23 = __builtin_amdgcn_perm(d3, d2, selA), p45 = __builtin_amdgcn_perm(d5, d4, selA), p67 = __builtin_amdgcn_perm(d7, d6, selA);
;         u32x2 o; o.x = __builtin_amdgcn_perm(p23, p01, 0x05040100u); o.y = __builtin_amdgcn_perm(p67, p45, 0x05040100u);
;         const int n = (lane >> 3) + 8 * j;
;         __builtin_nontemporal_store(o, (u32x2*)(dst + (size_t)n * 2048 + 8 * cc)); }
;     LDS_WAIT(); asm volatile("" ::: "memory");
; }
; __device__ __forceinline__ void cv_stash(const f32x4 (&t)[8], int lane, LAS unsigned* scr) {
;     const int lr = lane >> 3, c4 = lane & 7;
; #pragma unroll
;     for (int i = 0; i < 8; ++i) { const f32x4 v = t[i] * F8_WSCALE; scr[(8 * i + lr) * 9 + c4] = cvt4_fp8(v[0], v[1], v[2], v[3]); }
; }
.LBB0_1075:
	s_mov_b32 s98, 0
	s_cmp_lg_u32 s6, 0
	s_cselect_b64 s[4:5], -1, 0
	s_cmp_eq_u64 s[12:13], 0
	s_cselect_b64 s[0:1], -1, 0
	s_or_b64 s[0:1], s[4:5], s[0:1]
	s_and_b64 vcc, exec, s[0:1]
	s_cbranch_vccnz .LBB0_1077
	s_waitcnt vmcnt(7)
	v_pk_mul_f32 v[164:165], v[130:131], s[96:97] op_sel_hi:[1,0]
	v_cvt_pk_fp8_f32 v0, v164, v165
	s_waitcnt vmcnt(6)
	v_pk_mul_f32 v[164:165], v[134:135], s[96:97] op_sel_hi:[1,0]
	v_cvt_pk_fp8_f32 v167, v164, v165
	v_pk_mul_f32 v[162:163], v[132:133], s[96:97] op_sel_hi:[1,0]
	v_add_u32_e32 v166, v230, v231
	v_cvt_pk_fp8_f32 v0, v162, v163 op_sel:[0,0,1]
	v_pk_mul_f32 v[162:163], v[136:137], s[96:97] op_sel_hi:[1,0]
	s_waitcnt vmcnt(5)
	v_pk_mul_f32 v[164:165], v[138:139], s[96:97] op_sel_hi:[1,0]
	v_cvt_pk_fp8_f32 v167, v162, v163 op_sel:[0,0,1]
	v_pk_mul_f32 v[162:163], v[140:141], s[96:97] op_sel_hi:[1,0]
	ds_write2_b32 v166, v0, v167 offset1:72
	v_cvt_pk_fp8_f32 v0, v164, v165
	s_waitcnt vmcnt(4)
	v_pk_mul_f32 v[164:165], v[142:143], s[96:97] op_sel_hi:[1,0]
	v_cvt_pk_fp8_f32 v167, v164, v165
	v_cvt_pk_fp8_f32 v0, v162, v163 op_sel:[0,0,1]
	v_pk_mul_f32 v[162:163], v[144:145], s[96:97] op_sel_hi:[1,0]
	s_waitcnt vmcnt(3)
	v_pk_mul_f32 v[164:165], v[146:147], s[96:97] op_sel_hi:[1,0]
	v_cvt_pk_fp8_f32 v167, v162, v163 op_sel:[0,0,1]
	v_pk_mul_f32 v[162:163], v[148:149], s[96:97] op_sel_hi:[1,0]
	ds_write2_b32 v166, v0, v167 offset0:144 offset1:216
	v_cvt_pk_fp8_f32 v0, v164, v165
	s_waitcnt vmcnt(2)
	v_pk_mul_f32 v[164:165], v[150:151], s[96:97] op_sel_hi:[1,0]
	v_cvt_pk_fp8_f32 v167, v164, v165
	v_cvt_pk_fp8_f32 v0, v162, v163 op_sel:[0,0,1]
	v_pk_mul_f32 v[162:163], v[152:153], s[96:97] op_sel_hi:[1,0]
	v_add_u32_e32 v166, 0x400, v166
	v_cvt_pk_fp8_f32 v167, v162, v163 op_sel:[0,0,1]
	s_waitcnt vmcnt(1)
	v_pk_mul_f32 v[164:165], v[154:155], s[96:97] op_sel_hi:[1,0]
	v_pk_mul_f32 v[162:163], v[156:157], s[96:97] op_sel_hi:[1,0]
	ds_write2_b32 v166, v0, v167 offset0:32 offset1:104
	v_cvt_pk_fp8_f32 v0, v164, v165
	s_waitcnt vmcnt(0)
	v_pk_mul_f32 v[164:165], v[158:159], s[96:97] op_sel_hi:[1,0]
	v_cvt_pk_fp8_f32 v167, v164, v165
	v_cvt_pk_fp8_f32 v0, v162, v163 op_sel:[0,0,1]
	v_pk_mul_f32 v[162:163], v[160:161], s[96:97] op_sel_hi:[1,0]
	s_nop 0
	v_cvt_pk_fp8_f32 v167, v162, v163 op_sel:[0,0,1]
	v_lshl_add_u64 v[162:163], s[12:13], 0, v[182:183]
	v_lshl_add_u64 v[238:239], v[162:163], 0, v[184:185]
	ds_write2_b32 v166, v0, v167 offset0:176 offset1:248
	s_waitcnt lgkmcnt(0)
	v_add_u32_e32 v0, v229, v232
	ds_read2_b32 v[164:165], v0 offset0:18 offset1:20
	ds_read2_b32 v[166:167], v0 offset0:27 offset1:29
	ds_read2_b32 v[168:169], v0 offset0:36 offset1:38
	ds_read2_b32 v[170:171], v0 offset0:45 offset1:47
	ds_read2_b32 v[172:173], v0 offset0:54 offset1:56
	ds_read2_b32 v[174:175], v0 offset0:63 offset1:65
	ds_read2_b32 v[176:177], v0 offset1:2
	ds_read2_b32 v[234:235], v0 offset0:9 offset1:11
	s_waitcnt lgkmcnt(6)
	v_perm_b32 v164, v166, v164, v181
	s_waitcnt lgkmcnt(4)
	v_perm_b32 v166, v170, v168, v181
	s_waitcnt lgkmcnt(2)
	v_perm_b32 v168, v174, v172, v181
	v_perm_b32 v237, v168, v166, s90
	s_waitcnt lgkmcnt(0)
	v_perm_b32 v176, v234, v176, v181
	v_perm_b32 v236, v164, v176, s90
	v_perm_b32 v164, v235, v177, v181
	v_perm_b32 v165, v167, v165, v181
	v_perm_b32 v166, v171, v169, v181
	v_perm_b32 v167, v175, v173, v181
	v_perm_b32 v164, v165, v164, s90
	v_perm_b32 v165, v167, v166, s90
	v_lshl_add_u64 v[166:167], v[162:163], 0, v[188:189]
	global_store_dwordx2 v[238:239], v[236:237], off nt
	global_store_dwordx2 v[166:167], v[164:165], off nt
	ds_read2_b32 v[164:165], v0 offset0:22 offset1:24
	ds_read2_b32 v[166:167], v0 offset0:31 offset1:33
	ds_read2_b32 v[168:169], v0 offset0:40 offset1:42
	ds_read2_b32 v[170:171], v0 offset0:49 offset1:51
	ds_read2_b32 v[172:173], v0 offset0:58 offset1:60
	ds_read2_b32 v[174:175], v0 offset0:67 offset1:69
	ds_read2_b32 v[176:177], v0 offset0:4 offset1:6
	ds_read2_b32 v[234:235], v0 offset0:13 offset1:15
	s_waitcnt lgkmcnt(6)
	v_perm_b32 v164, v166, v164, v181
	s_waitcnt lgkmcnt(4)
	v_perm_b32 v166, v170, v168, v181
	s_waitcnt lgkmcnt(2)
	v_perm_b32 v168, v174, v172, v181
	v_perm_b32 v237, v168, v166, s90
	s_waitcnt lgkmcnt(0)
	v_perm_b32 v0, v234, v176, v181
	v_perm_b32 v236, v164, v0, s90
	v_perm_b32 v0, v235, v177, v181
	v_perm_b32 v164, v167, v165, v181
	v_perm_b32 v165, v171, v169, v181
	v_perm_b32 v166, v175, v173, v181
	v_lshl_add_u64 v[238:239], v[162:163], 0, v[186:187]
	v_perm_b32 v164, v164, v0, s90
	v_perm_b32 v165, v166, v165, s90
	v_lshl_add_u64 v[162:163], v[162:163], 0, v[190:191]
	global_store_dwordx2 v[238:239], v[236:237], off nt
	global_store_dwordx2 v[162:163], v[164:165], off nt
	s_waitcnt lgkmcnt(0)
.LBB0_1077:
	s_cmp_lg_u64 s[12:13], 0
	s_cselect_b64 s[0:1], -1, 0
	s_and_b64 s[2:3], s[4:5], s[0:1]
	v_cndmask_b32_e64 v0, 0, 1, s[2:3]
	v_cmp_ne_u32_e64 s[0:1], 1, v0
	s_andn2_b64 vcc, exec, s[2:3]
	s_cbranch_vccnz .LBB0_1079
	s_nop 0
	v_pk_mul_f32 v[162:163], v[130:131], s[96:97] op_sel_hi:[1,0]
	v_cvt_pk_fp8_f32 v0, v162, v163
	s_nop 0
	v_pk_mul_f32 v[162:163], v[134:135], s[96:97] op_sel_hi:[1,0]
	v_cvt_pk_fp8_f32 v164, v162, v163
	v_pk_mul_f32 v[162:163], v[132:133], s[96:97] op_sel_hi:[1,0]
	v_add_u32_e32 v165, v230, v231
	v_cvt_pk_fp8_f32 v0, v162, v163 op_sel:[0,0,1]
	v_pk_mul_f32 v[162:163], v[136:137], s[96:97] op_sel_hi:[1,0]
	v_cvt_pk_fp8_f32 v164, v162, v163 op_sel:[0,0,1]
	s_nop 0
	v_pk_mul_f32 v[162:163], v[138:139], s[96:97] op_sel_hi:[1,0]
	ds_write2_b32 v165, v0, v164 offset1:72
	v_cvt_pk_fp8_f32 v0, v162, v163
	s_nop 0
	v_pk_mul_f32 v[162:163], v[142:143], s[96:97] op_sel_hi:[1,0]
	v_cvt_pk_fp8_f32 v164, v162, v163
	v_pk_mul_f32 v[162:163], v[140:141], s[96:97] op_sel_hi:[1,0]
	v_cvt_pk_fp8_f32 v0, v162, v163 op_sel:[0,0,1]
	v_pk_mul_f32 v[162:163], v[144:145], s[96:97] op_sel_hi:[1,0]
	s_nop 0
	v_cvt_pk_fp8_f32 v164, v162, v163 op_sel:[0,0,1]
	s_nop 0
	v_pk_mul_f32 v[162:163], v[146:147], s[96:97] op_sel_hi:[1,0]
	ds_write2_b32 v165, v0, v164 offset0:144 offset1:216
	v_cvt_pk_fp8_f32 v166, v162, v163
	s_nop 0
	v_pk_mul_f32 v[162:163], v[150:151], s[96:97] op_sel_hi:[1,0]
	v_add_u32_e32 v0, 0x400, v165
	v_cvt_pk_fp8_f32 v167, v162, v163
	v_pk_mul_f32 v[162:163], v[148:149], s[96:97] op_sel_hi:[1,0]
	s_nop 0
	v_cvt_pk_fp8_f32 v166, v162, v163 op_sel:[0,0,1]
	v_pk_mul_f32 v[162:163], v[152:153], s[96:97] op_sel_hi:[1,0]
	s_nop 0
	v_cvt_pk_fp8_f32 v167, v162, v163 op_sel:[0,0,1]
	s_nop 0
	v_pk_mul_f32 v[162:163], v[154:155], s[96:97] op_sel_hi:[1,0]
	s_nop 0
	v_cvt_pk_fp8_f32 v168, v162, v163
	s_nop 0
	v_pk_mul_f32 v[162:163], v[158:159], s[96:97] op_sel_hi:[1,0]
	s_nop 0
	v_cvt_pk_fp8_f32 v169, v162, v163
	v_pk_mul_f32 v[162:163], v[156:157], s[96:97] op_sel_hi:[1,0]
	s_nop 0
	v_cvt_pk_fp8_f32 v168, v162, v163 op_sel:[0,0,1]
	v_pk_mul_f32 v[162:163], v[160:161], s[96:97] op_sel_hi:[1,0]
	s_nop 0
	v_cvt_pk_fp8_f32 v169, v162, v163 op_sel:[0,0,1]
	ds_write2_b32 v0, v166, v167 offset0:32 offset1:104
	ds_write2_b32 v0, v168, v169 offset0:176 offset1:248

; #define LAS __attribute__((address_space(3)))
; __device__ __forceinline__ unsigned cvt4_fp8(float a, float b, float c, float d) { int w = 0; w = __builtin_amdgcn_cvt_pk_fp8_f32(a, b, w, false); w = __builtin_amdgcn_cvt_pk_fp8_f32(c, d, w, true); return (unsigned)w; }
; __device__ __forceinline__ void cv_stash(const f32x4 (&t)[8], int lane, LAS unsigned* scr) {
;     const int lr = lane >> 3, c4 = lane & 7;
; #pragma unroll
;     for (int i = 0; i < 8; ++i) { const f32x4 v = t[i] * F8_WSCALE; scr[(8 * i + lr) * 9 + c4] = cvt4_fp8(v[0], v[1], v[2], v[3]); }
; }
.LBB0_1114:
	s_and_b64 vcc, exec, s[4:5]
	s_waitcnt lgkmcnt(0)
	s_barrier
	s_mov_b32 s98, 0
	s_cbranch_vccnz .LBB0_1152
	s_cmp_lg_u64 s[8:9], 0
	s_cselect_b64 s[14:15], -1, 0
	s_cmp_eq_u64 s[8:9], 0
	s_cbranch_scc1 .LBB0_1117
	s_nop 0
	v_pk_mul_f32 v[162:163], v[126:127], s[96:97] op_sel_hi:[1,0]
	v_cvt_pk_fp8_f32 v0, v162, v163
	s_nop 0
	v_pk_mul_f32 v[162:163], v[114:115], s[96:97] op_sel_hi:[1,0]
	v_cvt_pk_fp8_f32 v164, v162, v163
	v_pk_mul_f32 v[162:163], v[128:129], s[96:97] op_sel_hi:[1,0]
	v_add_u32_e32 v165, v230, v231
	v_cvt_pk_fp8_f32 v0, v162, v163 op_sel:[0,0,1]
	v_pk_mul_f32 v[162:163], v[116:117], s[96:97] op_sel_hi:[1,0]
	v_cvt_pk_fp8_f32 v164, v162, v163 op_sel:[0,0,1]
	s_nop 0
	v_pk_mul_f32 v[162:163], v[122:123], s[96:97] op_sel_hi:[1,0]
	ds_write2_b32 v165, v0, v164 offset1:72
	v_cvt_pk_fp8_f32 v0, v162, v163
	s_nop 0
	v_pk_mul_f32 v[162:163], v[106:107], s[96:97] op_sel_hi:[1,0]
	v_cvt_pk_fp8_f32 v164, v162, v163
	v_pk_mul_f32 v[162:163], v[124:125], s[96:97] op_sel_hi:[1,0]
	v_cvt_pk_fp8_f32 v0, v162, v163 op_sel:[0,0,1]
	v_pk_mul_f32 v[162:163], v[108:109], s[96:97] op_sel_hi:[1,0]
	s_nop 0
	v_cvt_pk_fp8_f32 v164, v162, v163 op_sel:[0,0,1]
	s_nop 0
	v_pk_mul_f32 v[162:163], v[118:119], s[96:97] op_sel_hi:[1,0]
	ds_write2_b32 v165, v0, v164 offset0:144 offset1:216
	v_cvt_pk_fp8_f32 v166, v162, v163
	s_nop 0
	v_pk_mul_f32 v[162:163], v[102:103], s[96:97] op_sel_hi:[1,0]
	v_add_u32_e32 v0, 0x400, v165
	v_cvt_pk_fp8_f32 v167, v162, v163
	v_pk_mul_f32 v[162:163], v[120:121], s[96:97] op_sel_hi:[1,0]
	s_nop 0
	v_cvt_pk_fp8_f32 v166, v162, v163 op_sel:[0,0,1]
	v_pk_mul_f32 v[162:163], v[104:105], s[96:97] op_sel_hi:[1,0]
	s_nop 0
	v_cvt_pk_fp8_f32 v167, v162, v163 op_sel:[0,0,1]
	s_nop 0
	v_pk_mul_f32 v[162:163], v[110:111], s[96:97] op_sel_hi:[1,0]
	s_nop 0
	v_cvt_pk_fp8_f32 v168, v162, v163
	s_nop 0
	v_pk_mul_f32 v[162:163], v[98:99], s[96:97] op_sel_hi:[1,0]
	s_nop 0
	v_cvt_pk_fp8_f32 v169, v162, v163
	v_pk_mul_f32 v[162:163], v[112:113], s[96:97] op_sel_hi:[1,0]
	s_nop 0
	v_cvt_pk_fp8_f32 v168, v162, v163 op_sel:[0,0,1]
	v_pk_mul_f32 v[162:163], v[100:101], s[96:97] op_sel_hi:[1,0]
	s_nop 0
	v_cvt_pk_fp8_f32 v169, v162, v163 op_sel:[0,0,1]
	ds_write2_b32 v0, v166, v167 offset0:32 offset1:104
	ds_write2_b32 v0, v168, v169 offset0:176 offset1:248

; #define PG8_BAR __builtin_amdgcn_s_barrier()
; template <bool F8 = false, class Epi, class Sched, class AB>
; __device__ __forceinline__ void gemm_phase(LAS unsigned char* lds, int KB, const Sched& S, const AB& P, const Epi& E, int wave_) {
;     ...
; #pragma unroll
;         for (int a = 0; a < 2; ++a)
; #pragma unroll
;             for (int b = 0; b < 2; ++b)
; #pragma unroll
;                 for (int m = 0; m < 4; ++m)
; #pragma unroll
;                     for (int n = 0; n < 2; ++n) acc[a][b][m][n] = (f32x4){0.f, 0.f, 0.f, 0.f};
;         cur = nxt; cA = nA; cB = nB; ++ui;
; #pragma unroll
;         for (int i = 0; i < 4; ++i) cvo[i] = nvo[i];
;         if (wr == 1) PG8_BAR;
.LBB0_1893:
	s_lshl_b32 s23, s30, 8
	s_lshl_b32 s30, s31, 8
	s_ashr_i32 s31, s30, 31
	s_or_b64 s[30:31], s[30:31], s[4:5]
	s_or_b32 s25, s23, 16
	s_or_b32 s54, s23, 32
	s_or_b32 s55, s23, 48
	s_or_b32 s56, s23, 0x80
	s_or_b32 s57, s23, 0x90
	s_or_b32 s58, s23, 0xa0
	s_or_b32 s59, s23, 0xb0
	s_add_u32 s60, s34, 0x100
	v_mov_b32_e32 v0, 0
	v_lshl_add_u64 v[158:159], s[28:29], 0, v[150:151]
	v_lshl_add_u64 v[160:161], s[28:29], 0, v[152:153]
	s_addc_u32 s61, s35, 0
	s_mov_b32 s62, -2
	s_mov_b64 s[34:35], 0
	v_mov_b64_e32 v[0:1], 0
	v_mov_b64_e32 v[2:3], 0
	v_mov_b64_e32 v[4:5], 0
	v_mov_b64_e32 v[6:7], 0
	v_mov_b64_e32 v[8:9], 0
	v_mov_b64_e32 v[10:11], 0
	v_mov_b64_e32 v[12:13], 0
	v_mov_b64_e32 v[14:15], 0
	v_mov_b64_e32 v[16:17], 0
	v_mov_b64_e32 v[18:19], 0
	v_mov_b64_e32 v[20:21], 0
	v_mov_b64_e32 v[22:23], 0
	v_mov_b64_e32 v[24:25], 0
	v_mov_b64_e32 v[26:27], 0
	v_mov_b64_e32 v[28:29], 0
	v_mov_b64_e32 v[30:31], 0
	v_mov_b64_e32 v[32:33], 0
	v_mov_b64_e32 v[34:35], 0
	v_mov_b64_e32 v[36:37], 0
	v_mov_b64_e32 v[38:39], 0
	v_mov_b64_e32 v[40:41], 0
	v_mov_b64_e32 v[42:43], 0
	v_mov_b64_e32 v[44:45], 0
	v_mov_b64_e32 v[46:47], 0
	v_mov_b64_e32 v[48:49], 0
	v_mov_b64_e32 v[50:51], 0
	v_mov_b64_e32 v[52:53], 0
	v_mov_b64_e32 v[54:55], 0
	v_mov_b64_e32 v[56:57], 0
	v_mov_b64_e32 v[58:59], 0
	v_mov_b64_e32 v[60:61], 0
	v_mov_b64_e32 v[62:63], 0
	v_mov_b64_e32 v[64:65], 0
	v_mov_b64_e32 v[66:67], 0
	v_mov_b64_e32 v[68:69], 0
	v_mov_b64_e32 v[70:71], 0
	v_mov_b64_e32 v[80:81], 0
	v_mov_b64_e32 v[82:83], 0
	v_mov_b64_e32 v[84:85], 0
	v_mov_b64_e32 v[86:87], 0
	s_waitcnt vmcnt(0)
	v_mov_b32_e32 v0, 0
	v_mov_b64_e32 v[72:73], 0
	v_mov_b64_e32 v[74:75], 0
	v_mov_b64_e32 v[76:77], 0
	v_mov_b64_e32 v[78:79], 0
	v_mov_b64_e32 v[88:89], 0
	v_mov_b64_e32 v[90:91], 0
	v_mov_b64_e32 v[92:93], 0
	v_mov_b64_e32 v[94:95], 0
	v_mov_b64_e32 v[96:97], 0
	v_mov_b64_e32 v[98:99], 0
	v_mov_b64_e32 v[100:101], 0
	v_mov_b64_e32 v[102:103], 0
	v_mov_b64_e32 v[104:105], 0
	v_mov_b64_e32 v[106:107], 0
	v_mov_b64_e32 v[108:109], 0
	v_mov_b64_e32 v[110:111], 0
	v_mov_b64_e32 v[112:113], 0
	v_mov_b64_e32 v[114:115], 0
	v_mov_b64_e32 v[116:117], 0
	v_mov_b64_e32 v[118:119], 0
	v_mov_b64_e32 v[120:121], 0
	v_mov_b64_e32 v[122:123], 0
	v_mov_b64_e32 v[124:125], 0
	v_mov_b64_e32 v[126:127], 0
	s_branch .LBB0_1895

; #define PG8_BAR __builtin_amdgcn_s_barrier()
; template <bool F8 = false, class Epi, class Sched, class AB>
; __device__ __forceinline__ void gemm_phase(LAS unsigned char* lds, int KB, const Sched& S, const AB& P, const Epi& E, int wave_) {
;     ...
; #pragma unroll
;         for (int a = 0; a < 2; ++a)
; #pragma unroll
;             for (int b = 0; b < 2; ++b)
; #pragma unroll
;                 for (int m = 0; m < 4; ++m)
; #pragma unroll
;                     for (int n = 0; n < 2; ++n) acc[a][b][m][n] = (f32x4){0.f, 0.f, 0.f, 0.f};
;         cur = nxt; cA = nA; cB = nB; ++ui;
; #pragma unroll
;         for (int i = 0; i < 4; ++i) cvo[i] = nvo[i];
;         if (wr == 1) PG8_BAR;
.LBB0_1978:
	s_add_u32 s24, s24, 0x80
	s_addc_u32 s25, s25, 0
	s_add_u32 s17, s26, 0x100
	v_mov_b32_e32 v32, 0
	s_addc_u32 s19, s27, 0
	s_mov_b32 s46, -2
	v_mov_b64_e32 v[32:33], 0
	v_mov_b64_e32 v[34:35], 0
	v_mov_b64_e32 v[36:37], 0
	v_mov_b64_e32 v[38:39], 0
	v_mov_b64_e32 v[40:41], 0
	v_mov_b64_e32 v[42:43], 0
	v_mov_b64_e32 v[44:45], 0
	v_mov_b64_e32 v[46:47], 0
	v_mov_b64_e32 v[48:49], 0
	v_mov_b64_e32 v[50:51], 0
	v_mov_b64_e32 v[52:53], 0
	v_mov_b64_e32 v[54:55], 0
	v_mov_b64_e32 v[56:57], 0
	v_mov_b64_e32 v[58:59], 0
	v_mov_b64_e32 v[60:61], 0
	v_mov_b64_e32 v[62:63], 0
	v_mov_b64_e32 v[64:65], 0
	v_mov_b64_e32 v[66:67], 0
	v_mov_b64_e32 v[68:69], 0
	v_mov_b64_e32 v[70:71], 0
	v_mov_b64_e32 v[72:73], 0
	v_mov_b64_e32 v[74:75], 0
	v_mov_b64_e32 v[76:77], 0
	v_mov_b64_e32 v[78:79], 0
	v_mov_b64_e32 v[80:81], 0
	v_mov_b64_e32 v[82:83], 0
	v_mov_b64_e32 v[84:85], 0
	v_mov_b64_e32 v[86:87], 0
	v_mov_b64_e32 v[88:89], 0
	v_mov_b64_e32 v[90:91], 0
	v_mov_b64_e32 v[92:93], 0
	v_mov_b64_e32 v[94:95], 0
	s_waitcnt vmcnt(0)
	v_mov_b32_e32 v32, 0
	v_mov_b64_e32 v[96:97], 0
	v_mov_b64_e32 v[98:99], 0
	v_mov_b64_e32 v[100:101], 0
	v_mov_b64_e32 v[102:103], 0
	v_mov_b64_e32 v[104:105], 0
	v_mov_b64_e32 v[106:107], 0
	v_mov_b64_e32 v[108:109], 0
	v_mov_b64_e32 v[110:111], 0
	v_mov_b64_e32 v[112:113], 0
	v_mov_b64_e32 v[114:115], 0
	v_mov_b64_e32 v[116:117], 0
	v_mov_b64_e32 v[118:119], 0
	v_mov_b64_e32 v[120:121], 0
	v_mov_b64_e32 v[122:123], 0
	v_mov_b64_e32 v[124:125], 0
	v_mov_b64_e32 v[126:127], 0
	v_mov_b64_e32 v[128:129], 0
	v_mov_b64_e32 v[130:131], 0
	v_mov_b64_e32 v[132:133], 0
	v_mov_b64_e32 v[134:135], 0
	v_mov_b64_e32 v[136:137], 0
	v_mov_b64_e32 v[138:139], 0
	v_mov_b64_e32 v[140:141], 0
	v_mov_b64_e32 v[142:143], 0
	v_mov_b64_e32 v[144:145], 0
	v_mov_b64_e32 v[146:147], 0
	v_mov_b64_e32 v[148:149], 0
	v_mov_b64_e32 v[150:151], 0
	v_mov_b64_e32 v[152:153], 0
	v_mov_b64_e32 v[154:155], 0
	v_mov_b64_e32 v[156:157], 0
	v_mov_b64_e32 v[158:159], 0

; #define PG8_BAR __builtin_amdgcn_s_barrier()
; template <bool F8 = false, class Epi, class Sched, class AB>
; __device__ __forceinline__ void gemm_phase(LAS unsigned char* lds, int KB, const Sched& S, const AB& P, const Epi& E, int wave_) {
;     ...
; #pragma unroll
;         for (int a = 0; a < 2; ++a)
; #pragma unroll
;             for (int b = 0; b < 2; ++b)
; #pragma unroll
;                 for (int m = 0; m < 4; ++m)
; #pragma unroll
;                     for (int n = 0; n < 2; ++n) acc[a][b][m][n] = (f32x4){0.f, 0.f, 0.f, 0.f};
;         cur = nxt; cA = nA; cB = nB; ++ui;
; #pragma unroll
;         for (int i = 0; i < 4; ++i) cvo[i] = nvo[i];
;         if (wr == 1) PG8_BAR;
.LBB0_2145:
	v_mov_b32_e32 v175, v161
	v_mov_b32_e32 v173, v161
	v_mov_b32_e32 v32, 0
	v_readlane_b32 s80, v254, 46
	v_lshl_add_u64 v[178:179], s[16:17], 0, v[172:173]
	v_lshl_add_u64 v[180:181], s[16:17], 0, v[174:175]
	v_lshl_add_u64 v[182:183], v[0:1], 0, s[22:23]
	s_mov_b32 s27, -2
	s_mov_b64 s[30:31], 0
	v_mov_b64_e32 v[32:33], 0
	v_mov_b64_e32 v[34:35], 0
	v_mov_b64_e32 v[36:37], 0
	v_mov_b64_e32 v[38:39], 0
	v_mov_b64_e32 v[40:41], 0
	v_mov_b64_e32 v[42:43], 0
	v_mov_b64_e32 v[44:45], 0
	v_mov_b64_e32 v[46:47], 0
	v_mov_b64_e32 v[48:49], 0
	v_mov_b64_e32 v[50:51], 0
	v_mov_b64_e32 v[52:53], 0
	v_mov_b64_e32 v[54:55], 0
	v_mov_b64_e32 v[56:57], 0
	v_mov_b64_e32 v[58:59], 0
	v_mov_b64_e32 v[60:61], 0
	v_mov_b64_e32 v[62:63], 0
	v_mov_b64_e32 v[64:65], 0
	v_mov_b64_e32 v[66:67], 0
	v_mov_b64_e32 v[68:69], 0
	v_mov_b64_e32 v[70:71], 0
	v_mov_b64_e32 v[72:73], 0
	v_mov_b64_e32 v[74:75], 0
	v_mov_b64_e32 v[76:77], 0
	v_mov_b64_e32 v[78:79], 0
	v_mov_b64_e32 v[80:81], 0
	v_mov_b64_e32 v[82:83], 0
	v_mov_b64_e32 v[84:85], 0
	v_mov_b64_e32 v[86:87], 0
	v_mov_b64_e32 v[88:89], 0
	v_mov_b64_e32 v[90:91], 0
	v_mov_b64_e32 v[92:93], 0
	v_mov_b64_e32 v[94:95], 0
	v_mov_b64_e32 v[96:97], 0
	v_mov_b64_e32 v[98:99], 0
	v_mov_b64_e32 v[100:101], 0
	v_mov_b64_e32 v[102:103], 0
	v_mov_b64_e32 v[104:105], 0
	v_mov_b64_e32 v[106:107], 0
	v_mov_b64_e32 v[108:109], 0
	v_mov_b64_e32 v[110:111], 0
	v_mov_b64_e32 v[112:113], 0
	v_mov_b64_e32 v[114:115], 0
	v_mov_b64_e32 v[116:117], 0
	v_mov_b64_e32 v[118:119], 0
	v_mov_b64_e32 v[120:121], 0
	v_mov_b64_e32 v[122:123], 0
	v_mov_b64_e32 v[124:125], 0
	v_mov_b64_e32 v[126:127], 0
	v_mov_b64_e32 v[128:129], 0
	v_mov_b64_e32 v[130:131], 0
	v_mov_b64_e32 v[132:133], 0
	v_mov_b64_e32 v[134:135], 0
	v_mov_b64_e32 v[136:137], 0
	v_mov_b64_e32 v[138:139], 0
	v_mov_b64_e32 v[140:141], 0
	v_mov_b64_e32 v[142:143], 0
	v_mov_b64_e32 v[144:145], 0
	v_mov_b64_e32 v[146:147], 0
	v_mov_b64_e32 v[148:149], 0
	v_mov_b64_e32 v[150:151], 0
	v_mov_b64_e32 v[152:153], 0
	v_mov_b64_e32 v[154:155], 0
	v_mov_b64_e32 v[156:157], 0
	v_mov_b64_e32 v[158:159], 0
	v_readlane_b32 s82, v254, 48
	v_readlane_b32 s83, v254, 49
	v_readlane_b32 s81, v254, 47

; #define PG8_BAR __builtin_amdgcn_s_barrier()
; template <bool F8 = false, class Epi, class Sched, class AB>
; __device__ __forceinline__ void gemm_phase(LAS unsigned char* lds, int KB, const Sched& S, const AB& P, const Epi& E, int wave_) {
;     ...
; #pragma unroll
;         for (int a = 0; a < 2; ++a)
; #pragma unroll
;             for (int b = 0; b < 2; ++b)
; #pragma unroll
;                 for (int m = 0; m < 4; ++m)
; #pragma unroll
;                     for (int n = 0; n < 2; ++n) acc[a][b][m][n] = (f32x4){0.f, 0.f, 0.f, 0.f};
;         cur = nxt; cA = nA; cB = nB; ++ui;
; #pragma unroll
;         for (int i = 0; i < 4; ++i) cvo[i] = nvo[i];
;         if (wr == 1) PG8_BAR;
.LBB0_2224:
	s_add_u32 s30, s30, 0x80
	v_mov_b32_e32 v32, 0
	s_addc_u32 s31, s31, 0
	v_lshl_add_u64 v[182:183], v[0:1], 0, s[16:17]
	s_mov_b32 s21, -2
	v_mov_b64_e32 v[32:33], 0
	v_mov_b64_e32 v[34:35], 0
	v_mov_b64_e32 v[36:37], 0
	v_mov_b64_e32 v[38:39], 0
	v_mov_b64_e32 v[40:41], 0
	v_mov_b64_e32 v[42:43], 0
	v_mov_b64_e32 v[44:45], 0
	v_mov_b64_e32 v[46:47], 0
	v_mov_b64_e32 v[48:49], 0
	v_mov_b64_e32 v[50:51], 0
	v_mov_b64_e32 v[52:53], 0
	v_mov_b64_e32 v[54:55], 0
	v_mov_b64_e32 v[56:57], 0
	v_mov_b64_e32 v[58:59], 0
	v_mov_b64_e32 v[60:61], 0
	v_mov_b64_e32 v[62:63], 0
	v_mov_b64_e32 v[64:65], 0
	v_mov_b64_e32 v[66:67], 0
	v_mov_b64_e32 v[68:69], 0
	v_mov_b64_e32 v[70:71], 0
	v_mov_b64_e32 v[72:73], 0
	v_mov_b64_e32 v[74:75], 0
	v_mov_b64_e32 v[76:77], 0
	v_mov_b64_e32 v[78:79], 0
	v_mov_b64_e32 v[80:81], 0
	v_mov_b64_e32 v[82:83], 0
	v_mov_b64_e32 v[84:85], 0
	v_mov_b64_e32 v[86:87], 0
	v_mov_b64_e32 v[88:89], 0
	v_mov_b64_e32 v[90:91], 0
	v_mov_b64_e32 v[92:93], 0
	v_mov_b64_e32 v[94:95], 0
	v_mov_b64_e32 v[96:97], 0
	v_mov_b64_e32 v[98:99], 0
	v_mov_b64_e32 v[100:101], 0
	v_mov_b64_e32 v[102:103], 0
	v_mov_b64_e32 v[104:105], 0
	v_mov_b64_e32 v[106:107], 0
	v_mov_b64_e32 v[108:109], 0
	v_mov_b64_e32 v[110:111], 0
	v_mov_b64_e32 v[112:113], 0
	v_mov_b64_e32 v[114:115], 0
	v_mov_b64_e32 v[116:117], 0
	v_mov_b64_e32 v[118:119], 0
	v_mov_b64_e32 v[120:121], 0
	v_mov_b64_e32 v[122:123], 0
	v_mov_b64_e32 v[124:125], 0
	v_mov_b64_e32 v[126:127], 0
	v_mov_b64_e32 v[128:129], 0
	v_mov_b64_e32 v[130:131], 0
	v_mov_b64_e32 v[132:133], 0
	v_mov_b64_e32 v[134:135], 0
	v_mov_b64_e32 v[136:137], 0
	v_mov_b64_e32 v[138:139], 0
	v_mov_b64_e32 v[140:141], 0
	v_mov_b64_e32 v[142:143], 0
	v_mov_b64_e32 v[144:145], 0
	v_mov_b64_e32 v[146:147], 0
	v_mov_b64_e32 v[148:149], 0
	v_mov_b64_e32 v[150:151], 0
	v_mov_b64_e32 v[152:153], 0
	v_mov_b64_e32 v[154:155], 0
	v_mov_b64_e32 v[156:157], 0
	v_mov_b64_e32 v[158:159], 0
